# loop-carried increments and exit test moved before the reduce barrier; no LDS wait at the loop head
# speedup vs baseline: 1.0104x; 1.0009x over previous
.LBB1_2:
	v_lshrrev_b32_e32 v151, 4, v137
	s_lshl_b64 s[6:7], s[2:3], 4
	v_cmp_eq_u32_e64 s[2:3], 1, v151
	s_waitcnt vmcnt(31)
	v_cvt_f16_f32_e32 v8, v8
	v_cmp_gt_u32_e32 vcc, 16, v137
	s_waitcnt vmcnt(29)
	v_cndmask_b32_e64 v116, 0, v116, s[2:3]
	s_waitcnt vmcnt(21)
	v_cndmask_b32_e64 v100, 0, v100, s[2:3]
	v_cmp_eq_u32_e64 s[0:1], 2, v151
	v_cndmask_b32_e64 v114, 0, v114, s[2:3]
	v_cndmask_b32_e64 v115, 0, v115, s[2:3]
	v_cndmask_b32_e32 v6, v116, v6, vcc
	v_cndmask_b32_e64 v116, 0, v117, s[2:3]
	v_cndmask_b32_e64 v108, 0, v108, s[2:3]
	v_cndmask_b32_e32 v26, v100, v26, vcc
	v_cvt_f16_f32_e32 v29, v29
	v_cndmask_b32_e64 v100, 0, v101, s[2:3]
	v_cndmask_b32_e32 v28, 0, v28, vcc
	v_cndmask_b32_e64 v152, 0, 1.0, s[0:1]
	v_cndmask_b32_e32 v114, v114, v120, vcc
	v_cndmask_b32_e32 v115, v115, v121, vcc
	v_cndmask_b32_e32 v7, v116, v7, vcc
	v_cndmask_b32_e64 v106, 0, v106, s[2:3]
	v_cndmask_b32_e64 v107, 0, v107, s[2:3]
	v_cndmask_b32_e32 v14, v108, v14, vcc
	v_cndmask_b32_e64 v108, 0, v109, s[2:3]
	v_cndmask_b32_e32 v27, v100, v27, vcc
	v_cvt_f16_f32_e32 v100, v28
	v_cndmask_b32_e32 v116, 0, v8, vcc
	v_cvt_pk_f16_f32 v8, v6, v7
	v_cvt_pk_f16_f32 v7, v114, v115
	v_cndmask_b32_e64 v114, v152, v140, s[2:3]
	v_cndmask_b32_e32 v106, v106, v112, vcc
	v_cndmask_b32_e32 v107, v107, v113, vcc
	v_cndmask_b32_e32 v15, v108, v15, vcc
	v_cndmask_b32_e64 v98, 0, v98, s[2:3]
	v_cndmask_b32_e64 v99, 0, v99, s[2:3]
	v_cndmask_b32_e32 v110, v114, v110, vcc
	v_cndmask_b32_e64 v114, 0, v141, s[2:3]
	v_cndmask_b32_e32 v108, 0, v16, vcc
	v_cvt_pk_f16_f32 v16, v14, v15
	v_cvt_pk_f16_f32 v15, v106, v107
	v_cndmask_b32_e64 v106, v152, v138, s[2:3]
	v_cndmask_b32_e32 v98, v98, v104, vcc
	v_cndmask_b32_e32 v99, v99, v105, vcc
	v_cndmask_b32_e32 v111, v114, v111, vcc
	v_cndmask_b32_e32 v102, v106, v102, vcc
	v_cndmask_b32_e64 v106, 0, v139, s[2:3]
	v_cndmask_b32_e32 v29, 0, v29, vcc
	v_cvt_pk_f16_f32 v28, v26, v27
	v_cvt_pk_f16_f32 v27, v98, v99
	v_lshlrev_b32_e32 v101, 10, v1
	v_bitop3_b32 v98, v151, v0, 3 bitop3:0x78
	v_lshl_add_u64 v[130:131], s[4:5], 0, v[130:131]
	v_cvt_f16_f32_e32 v4, v4
	v_cvt_pk_f16_f32 v14, v110, v111
	v_cndmask_b32_e32 v103, v106, v103, vcc
	v_pack_b32_f16 v29, v100, v29
	v_lshl_or_b32 v111, v98, 4, v101
	v_lshlrev_b32_e32 v100, 4, v1
	s_movk_i32 s4, 0xc0
	v_cndmask_b32_e64 v124, 0, v124, s[2:3]
	v_cvt_pk_f16_f32 v26, v102, v103
	v_and_b32_e32 v112, 0xc0, v100
	v_bitop3_b32 v100, v100, s4, v111 bitop3:0x26
	s_lshl_b32 s4, s20, 3
	v_lshrrev_b32_e32 v102, 5, v137
	v_lshrrev_b32_e32 v104, 1, v137
	v_cndmask_b32_e64 v122, 0, v122, s[2:3]
	v_cndmask_b32_e64 v123, 0, v123, s[2:3]
	v_cndmask_b32_e32 v2, v124, v2, vcc
	v_cvt_f16_f32_e32 v5, v5
	v_cndmask_b32_e64 v124, 0, v125, s[2:3]
	v_cvt_f16_f32_e32 v9, v9
	v_or_b32_e32 v103, s4, v102
	v_and_or_b32 v110, v104, 8, v101
	v_bitop3_b32 v101, s4, v1, v102 bitop3:0x36
	s_lshl_b32 s4, s20, 4
	v_cndmask_b32_e32 v122, v122, v128, vcc
	v_cndmask_b32_e32 v123, v123, v129, vcc
	v_cndmask_b32_e32 v3, v124, v3, vcc
	v_cndmask_b32_e32 v17, 0, v17, vcc
	v_lshlrev_b32_e32 v107, 4, v101
	v_bitop3_b32 v101, v103, v1, 2 bitop3:0x36
	s_add_i32 s4, s4, 0x10000
	v_bfe_u32 v0, v0, 4, 2
	v_cndmask_b32_e64 v144, v152, v144, s[2:3]
	v_cndmask_b32_e32 v124, 0, v4, vcc
	v_cvt_pk_f16_f32 v4, v2, v3
	v_cvt_pk_f16_f32 v3, v122, v123
	v_cndmask_b32_e64 v122, v152, v142, s[2:3]
	v_cvt_pk_f16_f32 v17, v108, v17
	s_movk_i32 s5, 0x80
	v_lshlrev_b32_e32 v108, 4, v101
	v_bitop3_b32 v101, v103, v1, 4 bitop3:0x36
	s_cmp_lt_u32 s22, 64
	v_lshlrev_b32_e32 v104, 5, v0
	v_lshlrev_b32_e32 v0, 6, v0
	v_cndmask_b32_e32 v126, v144, v126, vcc
	v_cndmask_b32_e64 v144, 0, v145, s[2:3]
	v_cndmask_b32_e32 v118, v122, v118, vcc
	v_cndmask_b32_e64 v122, 0, v143, s[2:3]
	v_bitop3_b32 v99, v112, s5, v111 bitop3:0x36
	v_lshlrev_b32_e32 v109, 4, v101
	v_bitop3_b32 v101, v103, v1, 6 bitop3:0x36
	v_lshl_or_b32 v105, s20, 8, v0
	v_mov_b32_e32 v0, 0x1ec00
	s_cselect_b64 s[4:5], -1, 0
	v_cndmask_b32_e32 v127, v144, v127, vcc
	v_cndmask_b32_e32 v5, 0, v5, vcc
	v_cndmask_b32_e32 v119, v122, v119, vcc
	v_cndmask_b32_e32 v9, 0, v9, vcc
	v_lshlrev_b32_e32 v113, 4, v101
	v_lshlrev_b32_e32 v101, 5, v1
	v_lshl_add_u32 v106, v137, 6, v0
	s_cmp_eq_u32 s20, 0
	s_cselect_b32 s31, 0, 0xffff1d00
	v_add_u32_e32 v106, s31, v106
	v_cndmask_b32_e64 v0, 0, 1, s[4:5]
	v_lshl_add_u64 v[132:133], s[8:9], 0, v[132:133]
	v_or_b32_e32 v148, 0x400, v147
	v_or_b32_e32 v149, 0x800, v147
	v_or_b32_e32 v150, 0xc00, v147
	v_cvt_pk_f16_f32 v2, v126, v127
	v_pack_b32_f16 v5, v124, v5
	v_cvt_pk_f16_f32 v6, v118, v119
	v_pack_b32_f16 v9, v116, v9
	v_bitop3_b32 v98, v112, 64, v111 bitop3:0x36
	v_lshl_or_b32 v104, s20, 7, v104
	s_mov_b32 s22, 0x98000
	s_mov_b32 s23, 0x5040100
	s_mov_b32 s24, 0x7060302
	v_add_u32_e32 v107, v107, v110
	v_add_u32_e32 v108, v108, v110
	v_add_u32_e32 v109, v109, v110
	v_add_u32_e32 v110, v113, v110
	v_add_u32_e32 v111, v112, v111
	v_lshlrev_b32_e32 v113, 4, v137
	v_or_b32_e32 v113, 0x10000, v113
	s_lshr_b32 s28, s20, 2
	s_and_b32 s29, s20, 3
	s_lshl_b32 s28, s28, 10
	s_lshl_b32 s29, s29, 2
	s_add_i32 s28, s28, s29
	v_add_u32_e32 v112, s28, v113
	v_cmp_eq_u32_e64 s[26:27], 3, v151
	v_add_u32_e32 v114, 0x12400, v101
	v_and_b32_e32 v108, 15, v137
	s_lshl_b32 s31, s20, 3
	v_add_u32_e32 v107, s31, v151
	v_xor_b32_e32 v107, v107, v108
	v_lshlrev_b32_e32 v107, 4, v107
	v_lshl_or_b32 v107, v108, 10, v107
	v_xor_b32_e32 v108, 64, v107
	v_cmp_ne_u32_e64 s[4:5], 1, v0
	s_waitcnt vmcnt(16)
	v_cndmask_b32_e64 v1, v30, v134, s[0:1]
	v_bfi_b32 v30, s10, v1, v30
	v_perm_b32 v1, v22, v134, s24
	v_cndmask_b32_e64 v22, v22, v1, s[0:1]
	v_bfi_b32 v1, s10, v135, v18
	v_perm_b32 v121, v10, v135, s24
	v_cndmask_b32_e64 v18, v18, v1, s[0:1]
	v_cndmask_b32_e64 v10, v10, v121, s[0:1]
	v_mov_b32_e32 v121, v136
	v_mov_b32_e32 v144, v136
	v_mov_b32_e32 v145, v136
	v_mov_b32_e32 v0, v136
	v_mov_b32_e32 v1, v136
	s_waitcnt lgkmcnt(0)
	s_barrier
	ds_read_u16 v102, v114
	ds_read_u16 v103, v114 offset:512
	ds_read_u16 v115, v114 offset:1024
	ds_read_u16 v116, v114 offset:1536
	v_add_u32_e32 v0, 0x12c00, v105
	ds_read_b128 v[240:243], v0
	ds_read_b128 v[244:247], v0 offset:16
	ds_read_b128 v[248:251], v0 offset:32
	ds_read_b128 v[252:255], v0 offset:48
	v_add_u32_e32 v114, 2, v114
	s_waitcnt lgkmcnt(0)
	s_branch .LBB1_4
.LBB1_4:
	s_and_saveexec_b64 s[8:9], s[2:3]
	v_perm_b32 v5, v1, v102, s23
	v_perm_b32 v9, v121, v103, s23
	v_perm_b32 v17, v144, v115, s23
	v_perm_b32 v29, v145, v116, s23
	s_or_b64 exec, exec, s[8:9]
	v_mfma_f32_16x16x32_f16 v[152:155], v[30:33], v[2:5], 0
	v_mfma_f32_16x16x32_f16 v[168:171], v[22:25], v[2:5], 0
	s_cmp_lg_u32 s22, 0x818000
	v_mfma_f32_16x16x32_f16 v[156:159], v[30:33], v[6:9], 0
	v_mfma_f32_16x16x32_f16 v[172:175], v[22:25], v[6:9], 0
	s_cselect_b32 s9, s11, 15
	v_mfma_f32_16x16x32_f16 v[160:163], v[30:33], v[14:17], 0
	v_mfma_f32_16x16x32_f16 v[176:179], v[22:25], v[14:17], 0
	v_mfma_f32_16x16x32_f16 v[164:167], v[30:33], v[26:29], 0
	v_mfma_f32_16x16x32_f16 v[180:183], v[22:25], v[26:29], 0
	v_mfma_f32_16x16x32_f16 v[184:187], v[18:21], v[2:5], 0
	v_cvt_pk_f16_f32 v216, v152, v153
	v_cvt_pk_f16_f32 v217, v154, v155
	v_pk_max_f16 v216, v216, 0
	v_pk_max_f16 v217, v217, 0
	v_cvt_pk_f16_f32 v218, v168, v169
	v_cvt_pk_f16_f32 v219, v170, v171
	v_pk_max_f16 v218, v218, 0
	v_pk_max_f16 v219, v219, 0
	ds_write_b128 v107, v[216:219]
	v_mfma_f32_16x16x32_f16 v[200:203], v[10:13], v[2:5], 0
	v_cvt_pk_f16_f32 v220, v156, v157
	v_cvt_pk_f16_f32 v221, v158, v159
	v_pk_max_f16 v220, v220, 0
	v_pk_max_f16 v221, v221, 0
	v_cvt_pk_f16_f32 v222, v172, v173
	v_cvt_pk_f16_f32 v223, v174, v175
	v_pk_max_f16 v222, v222, 0
	v_pk_max_f16 v223, v223, 0
	ds_write_b128 v107, v[220:223] offset:16384
	v_mfma_f32_16x16x32_f16 v[188:191], v[18:21], v[6:9], 0
	v_cvt_pk_f16_f32 v224, v160, v161
	v_cvt_pk_f16_f32 v225, v162, v163
	v_pk_max_f16 v224, v224, 0
	v_pk_max_f16 v225, v225, 0
	v_cvt_pk_f16_f32 v226, v176, v177
	v_cvt_pk_f16_f32 v227, v178, v179
	v_pk_max_f16 v226, v226, 0
	v_pk_max_f16 v227, v227, 0
	ds_write_b128 v107, v[224:227] offset:32768
	v_mfma_f32_16x16x32_f16 v[204:207], v[10:13], v[6:9], 0
	v_cvt_pk_f16_f32 v228, v164, v165
	v_cvt_pk_f16_f32 v229, v166, v167
	v_pk_max_f16 v228, v228, 0
	v_pk_max_f16 v229, v229, 0
	v_cvt_pk_f16_f32 v230, v180, v181
	v_cvt_pk_f16_f32 v231, v182, v183
	v_pk_max_f16 v230, v230, 0
	v_pk_max_f16 v231, v231, 0
	ds_write_b128 v107, v[228:231] offset:49152
	v_mfma_f32_16x16x32_f16 v[192:195], v[18:21], v[14:17], 0
	v_cvt_pk_f16_f32 v232, v184, v185
	v_cvt_pk_f16_f32 v233, v186, v187
	v_pk_max_f16 v232, v232, 0
	v_pk_max_f16 v233, v233, 0
	v_cvt_pk_f16_f32 v234, v200, v201
	v_cvt_pk_f16_f32 v235, v202, v203
	v_pk_max_f16 v234, v234, 0
	v_pk_max_f16 v235, v235, 0
	ds_write_b128 v108, v[232:235]
	v_mfma_f32_16x16x32_f16 v[208:211], v[10:13], v[14:17], 0
	v_cvt_pk_f16_f32 v236, v188, v189
	v_cvt_pk_f16_f32 v237, v190, v191
	v_pk_max_f16 v236, v236, 0
	v_pk_max_f16 v237, v237, 0
	v_cvt_pk_f16_f32 v238, v204, v205
	v_cvt_pk_f16_f32 v239, v206, v207
	v_pk_max_f16 v238, v238, 0
	v_pk_max_f16 v239, v239, 0
	ds_write_b128 v108, v[236:239] offset:16384
	v_mfma_f32_16x16x32_f16 v[196:199], v[18:21], v[26:29], 0
	v_mfma_f32_16x16x32_f16 v[212:215], v[10:13], v[26:29], 0
	v_cvt_pk_f16_f32 v122, v192, v193
	v_cvt_pk_f16_f32 v123, v194, v195
	v_pk_max_f16 v122, v122, 0
	v_pk_max_f16 v123, v123, 0
	v_cvt_pk_f16_f32 v124, v208, v209
	v_cvt_pk_f16_f32 v125, v210, v211
	v_pk_max_f16 v124, v124, 0
	v_pk_max_f16 v125, v125, 0
	ds_write_b128 v108, v[122:125] offset:32768
	v_cvt_pk_f16_f32 v126, v196, v197
	v_cvt_pk_f16_f32 v127, v198, v199
	v_pk_max_f16 v126, v126, 0
	v_pk_max_f16 v127, v127, 0
	v_cvt_pk_f16_f32 v128, v212, v213
	v_cvt_pk_f16_f32 v129, v214, v215
	v_pk_max_f16 v128, v128, 0
	v_pk_max_f16 v129, v129, 0
	ds_write_b128 v108, v[126:129] offset:49152
	s_waitcnt lgkmcnt(0)
	s_barrier
	ds_read_b128 v[122:125], v111
	ds_read_b128 v[126:129], v111 offset:16384
	ds_read_b128 v[134:137], v111 offset:32768
	ds_read_b128 v[138:141], v111 offset:49152
	ds_read_b128 v[142:145], v98
	ds_read_b128 v[152:155], v98 offset:16384
	ds_read_b128 v[156:159], v98 offset:32768
	ds_read_b128 v[160:163], v98 offset:49152
	s_lshl_b32 s20, s9, 7
	v_lshl_add_u64 v[0:1], s[20:21], 3, v[132:133]
	s_add_i32 s25, s22, 0xfff88000
	s_lshl_b32 s8, s9, 8
	buffer_load_dwordx4 v[192:195], v147, s[16:19], s25 offen
	buffer_load_dwordx4 v[196:199], v148, s[16:19], s25 offen
	buffer_load_dwordx4 v[200:203], v149, s[16:19], s25 offen
	buffer_load_dwordx4 v[204:207], v150, s[16:19], s25 offen
	s_waitcnt vmcnt(19) lgkmcnt(7)
	v_mfma_f32_16x16x32_f16 v[164:167], v[58:61], v[122:125], v[240:243]
	s_waitcnt lgkmcnt(6)
	v_mfma_f32_16x16x32_f16 v[168:171], v[58:61], v[126:129], v[240:243]
	s_waitcnt lgkmcnt(5)
	v_mfma_f32_16x16x32_f16 v[172:175], v[58:61], v[134:137], v[240:243]
	s_waitcnt lgkmcnt(4)
	v_mfma_f32_16x16x32_f16 v[10:13], v[58:61], v[138:141], v[240:243]
	s_waitcnt vmcnt(18)
	v_mfma_f32_16x16x32_f16 v[58:61], v[54:57], v[122:125], v[244:247]
	v_mfma_f32_16x16x32_f16 v[176:179], v[54:57], v[126:129], v[244:247]
	v_mfma_f32_16x16x32_f16 v[180:183], v[54:57], v[134:137], v[244:247]
	v_mfma_f32_16x16x32_f16 v[18:21], v[54:57], v[138:141], v[244:247]
	s_waitcnt vmcnt(17)
	v_mfma_f32_16x16x32_f16 v[54:57], v[50:53], v[122:125], v[248:251]
	v_mfma_f32_16x16x32_f16 v[184:187], v[50:53], v[126:129], v[248:251]
	v_mfma_f32_16x16x32_f16 v[188:191], v[50:53], v[134:137], v[248:251]
	v_mfma_f32_16x16x32_f16 v[22:25], v[50:53], v[138:141], v[248:251]
	s_waitcnt vmcnt(16)
	v_mfma_f32_16x16x32_f16 v[50:53], v[38:41], v[122:125], v[252:255]
	v_mfma_f32_16x16x32_f16 v[122:125], v[38:41], v[126:129], v[252:255]
	v_mfma_f32_16x16x32_f16 v[126:129], v[38:41], v[134:137], v[252:255]
	v_mfma_f32_16x16x32_f16 v[38:41], v[38:41], v[138:141], v[252:255]
	ds_read_b128 v[136:139], v99
	ds_read_b128 v[208:211], v99 offset:16384
	ds_read_b128 v[212:215], v99 offset:32768
	ds_read_b128 v[216:219], v99 offset:49152
	s_add_i32 s9, s22, 0xfff90000
	s_waitcnt vmcnt(15) lgkmcnt(7)
	v_mfma_f32_16x16x32_f16 v[164:167], v[94:97], v[142:145], v[164:167]
	s_waitcnt lgkmcnt(6)
	v_mfma_f32_16x16x32_f16 v[168:171], v[94:97], v[152:155], v[168:171]
	s_waitcnt vmcnt(14)
	v_mfma_f32_16x16x32_f16 v[58:61], v[90:93], v[142:145], v[58:61]
	v_mfma_f32_16x16x32_f16 v[176:179], v[90:93], v[152:155], v[176:179]
	s_waitcnt vmcnt(13)
	v_mfma_f32_16x16x32_f16 v[54:57], v[78:81], v[142:145], v[54:57]
	v_mfma_f32_16x16x32_f16 v[184:187], v[78:81], v[152:155], v[184:187]
	s_waitcnt vmcnt(12)
	v_mfma_f32_16x16x32_f16 v[50:53], v[34:37], v[142:145], v[50:53]
	buffer_load_dwordx4 v[140:143], v147, s[16:19], s9 offen
	buffer_load_dwordx4 v[220:223], v148, s[16:19], s9 offen
	v_mfma_f32_16x16x32_f16 v[122:125], v[34:37], v[152:155], v[122:125]
	buffer_load_dwordx4 v[152:155], v149, s[16:19], s9 offen
	buffer_load_dwordx4 v[224:227], v150, s[16:19], s9 offen
	s_mov_b32 s9, s21
	s_waitcnt lgkmcnt(5)
	v_mfma_f32_16x16x32_f16 v[172:175], v[94:97], v[156:159], v[172:175]
	s_waitcnt lgkmcnt(4)
	v_mfma_f32_16x16x32_f16 v[94:97], v[94:97], v[160:163], v[10:13]
	s_nop 2
	v_lshl_add_u64 v[10:11], s[8:9], 4, v[130:131]
	v_mfma_f32_16x16x32_f16 v[180:183], v[90:93], v[156:159], v[180:183]
	v_mfma_f32_16x16x32_f16 v[90:93], v[90:93], v[160:163], v[18:21]
	v_mfma_f32_16x16x32_f16 v[188:191], v[78:81], v[156:159], v[188:191]
	v_mfma_f32_16x16x32_f16 v[78:81], v[78:81], v[160:163], v[22:25]
	global_load_dwordx4 v[30:33], v[10:11], off
	s_nop 1
	global_load_dwordx4 v[22:25], v[10:11], off offset:1024
	global_load_dwordx4 v[18:21], v[10:11], off offset:2048
	s_nop 0
	global_load_dwordx4 v[10:13], v[10:11], off offset:3072
	s_nop 0
	global_load_dwordx2 v[134:135], v[0:1], off
	v_mfma_f32_16x16x32_f16 v[126:129], v[34:37], v[156:159], v[126:129]
	v_mfma_f32_16x16x32_f16 v[34:37], v[34:37], v[160:163], v[38:41]
	s_nop 2
	ds_read_b128 v[38:41], v100
	ds_read_b128 v[156:159], v100 offset:16384
	ds_read_b128 v[160:163], v100 offset:32768
	ds_read_b128 v[228:231], v100 offset:49152
	s_add_i32 s8, s22, 0xfff98000
	s_waitcnt vmcnt(20) lgkmcnt(7)
	v_mfma_f32_16x16x32_f16 v[164:167], v[82:85], v[136:139], v[164:167]
	s_waitcnt lgkmcnt(6)
	v_mfma_f32_16x16x32_f16 v[168:171], v[82:85], v[208:211], v[168:171]
	s_waitcnt lgkmcnt(5)
	v_mfma_f32_16x16x32_f16 v[172:175], v[82:85], v[212:215], v[172:175]
	s_waitcnt lgkmcnt(4)
	v_mfma_f32_16x16x32_f16 v[82:85], v[82:85], v[216:219], v[94:97]
	s_waitcnt vmcnt(19)
	v_mfma_f32_16x16x32_f16 v[58:61], v[70:73], v[136:139], v[58:61]
	v_mfma_f32_16x16x32_f16 v[94:97], v[70:73], v[208:211], v[176:179]
	v_mfma_f32_16x16x32_f16 v[176:179], v[70:73], v[212:215], v[180:183]
	v_mfma_f32_16x16x32_f16 v[70:73], v[70:73], v[216:219], v[90:93]
	s_waitcnt vmcnt(18)
	v_mfma_f32_16x16x32_f16 v[54:57], v[62:65], v[136:139], v[54:57]
	v_mfma_f32_16x16x32_f16 v[90:93], v[62:65], v[208:211], v[184:187]
	v_mfma_f32_16x16x32_f16 v[180:183], v[62:65], v[212:215], v[188:191]
	v_mfma_f32_16x16x32_f16 v[62:65], v[62:65], v[216:219], v[78:81]
	s_waitcnt vmcnt(17)
	v_mfma_f32_16x16x32_f16 v[50:53], v[42:45], v[136:139], v[50:53]
	v_mfma_f32_16x16x32_f16 v[78:81], v[42:45], v[208:211], v[122:125]
	v_mfma_f32_16x16x32_f16 v[122:125], v[42:45], v[212:215], v[126:129]
	s_nop 2
	buffer_load_dwordx4 v[126:129], v147, s[16:19], s8 offen
	buffer_load_dwordx4 v[136:139], v148, s[16:19], s8 offen
	buffer_load_dwordx4 v[184:187], v149, s[16:19], s8 offen
	buffer_load_dwordx4 v[188:191], v150, s[16:19], s8 offen
	v_mfma_f32_16x16x32_f16 v[34:37], v[42:45], v[216:219], v[34:37]
	ds_read_b128 v[42:45], v111 offset:256
	ds_read_b128 v[208:211], v111 offset:16640
	ds_read_b128 v[212:215], v111 offset:33024
	ds_read_b128 v[216:219], v111 offset:49408
	s_add_i32 s8, s22, 0xfffa0000
	s_waitcnt vmcnt(20) lgkmcnt(7)
	v_mfma_f32_16x16x32_f16 v[164:167], v[86:89], v[38:41], v[164:167]
	s_waitcnt lgkmcnt(6)
	v_mfma_f32_16x16x32_f16 v[168:171], v[86:89], v[156:159], v[168:171]
	s_waitcnt lgkmcnt(5)
	v_mfma_f32_16x16x32_f16 v[172:175], v[86:89], v[160:163], v[172:175]
	s_waitcnt lgkmcnt(4)
	v_mfma_f32_16x16x32_f16 v[82:85], v[86:89], v[228:231], v[82:85]
	s_waitcnt vmcnt(19)
	v_mfma_f32_16x16x32_f16 v[58:61], v[74:77], v[38:41], v[58:61]
	v_mfma_f32_16x16x32_f16 v[86:89], v[74:77], v[156:159], v[94:97]
	v_mfma_f32_16x16x32_f16 v[94:97], v[74:77], v[160:163], v[176:179]
	v_mfma_f32_16x16x32_f16 v[70:73], v[74:77], v[228:231], v[70:73]
	s_waitcnt vmcnt(18)
	v_mfma_f32_16x16x32_f16 v[54:57], v[66:69], v[38:41], v[54:57]
	v_mfma_f32_16x16x32_f16 v[74:77], v[66:69], v[156:159], v[90:93]
	v_mfma_f32_16x16x32_f16 v[90:93], v[66:69], v[160:163], v[180:183]
	v_mfma_f32_16x16x32_f16 v[62:65], v[66:69], v[228:231], v[62:65]
	s_waitcnt vmcnt(17)
	v_mfma_f32_16x16x32_f16 v[38:41], v[46:49], v[38:41], v[50:53]
	v_mfma_f32_16x16x32_f16 v[50:53], v[46:49], v[156:159], v[78:81]
	v_mfma_f32_16x16x32_f16 v[66:69], v[46:49], v[160:163], v[122:125]
	s_nop 1
	buffer_load_dwordx4 v[78:81], v147, s[16:19], s8 offen
	buffer_load_dwordx4 v[122:125], v148, s[16:19], s8 offen
	buffer_load_dwordx4 v[156:159], v149, s[16:19], s8 offen
	buffer_load_dwordx4 v[160:163], v150, s[16:19], s8 offen
	v_mfma_f32_16x16x32_f16 v[34:37], v[46:49], v[228:231], v[34:37]
	ds_read_b128 v[46:49], v98 offset:256
	ds_read_b128 v[176:179], v98 offset:16640
	ds_read_b128 v[180:183], v98 offset:33024
	ds_read_b128 v[228:231], v98 offset:49408
	s_add_i32 s8, s22, 0xfffa8000
	s_waitcnt vmcnt(20) lgkmcnt(7)
	v_mfma_f32_16x16x32_f16 v[164:167], v[192:195], v[42:45], v[164:167]
	s_waitcnt lgkmcnt(6)
	v_mfma_f32_16x16x32_f16 v[168:171], v[192:195], v[208:211], v[168:171]
	s_waitcnt lgkmcnt(5)
	v_mfma_f32_16x16x32_f16 v[172:175], v[192:195], v[212:215], v[172:175]
	s_waitcnt lgkmcnt(4)
	v_mfma_f32_16x16x32_f16 v[82:85], v[192:195], v[216:219], v[82:85]
	s_waitcnt vmcnt(19)
	v_mfma_f32_16x16x32_f16 v[58:61], v[196:199], v[42:45], v[58:61]
	v_mfma_f32_16x16x32_f16 v[86:89], v[196:199], v[208:211], v[86:89]
	v_mfma_f32_16x16x32_f16 v[94:97], v[196:199], v[212:215], v[94:97]
	v_mfma_f32_16x16x32_f16 v[70:73], v[196:199], v[216:219], v[70:73]
	s_waitcnt vmcnt(18)
	v_mfma_f32_16x16x32_f16 v[54:57], v[200:203], v[42:45], v[54:57]
	v_mfma_f32_16x16x32_f16 v[74:77], v[200:203], v[208:211], v[74:77]
	v_mfma_f32_16x16x32_f16 v[90:93], v[200:203], v[212:215], v[90:93]
	v_mfma_f32_16x16x32_f16 v[62:65], v[200:203], v[216:219], v[62:65]
	s_waitcnt vmcnt(17)
	v_mfma_f32_16x16x32_f16 v[38:41], v[204:207], v[42:45], v[38:41]
	v_mfma_f32_16x16x32_f16 v[42:45], v[204:207], v[208:211], v[50:53]
	v_mfma_f32_16x16x32_f16 v[50:53], v[204:207], v[212:215], v[66:69]
	s_nop 2
	buffer_load_dwordx4 v[66:69], v147, s[16:19], s8 offen
	buffer_load_dwordx4 v[192:195], v148, s[16:19], s8 offen
	buffer_load_dwordx4 v[196:199], v149, s[16:19], s8 offen
	buffer_load_dwordx4 v[200:203], v150, s[16:19], s8 offen
	v_mfma_f32_16x16x32_f16 v[34:37], v[204:207], v[216:219], v[34:37]
	ds_read_b128 v[204:207], v99 offset:256
	ds_read_b128 v[208:211], v99 offset:16640
	ds_read_b128 v[212:215], v99 offset:33024
	ds_read_b128 v[216:219], v99 offset:49408
	s_add_i32 s8, s22, 0xfffb0000
	s_waitcnt vmcnt(20) lgkmcnt(7)
	v_mfma_f32_16x16x32_f16 v[164:167], v[140:143], v[46:49], v[164:167]
	s_waitcnt lgkmcnt(6)
	v_mfma_f32_16x16x32_f16 v[168:171], v[140:143], v[176:179], v[168:171]
	s_waitcnt lgkmcnt(5)
	v_mfma_f32_16x16x32_f16 v[172:175], v[140:143], v[180:183], v[172:175]
	s_waitcnt lgkmcnt(4)
	v_mfma_f32_16x16x32_f16 v[82:85], v[140:143], v[228:231], v[82:85]
	s_waitcnt vmcnt(19)
	v_mfma_f32_16x16x32_f16 v[58:61], v[220:223], v[46:49], v[58:61]
	v_mfma_f32_16x16x32_f16 v[86:89], v[220:223], v[176:179], v[86:89]
	s_waitcnt vmcnt(18)
	v_mfma_f32_16x16x32_f16 v[54:57], v[152:155], v[46:49], v[54:57]
	v_mfma_f32_16x16x32_f16 v[74:77], v[152:155], v[176:179], v[74:77]
	v_mfma_f32_16x16x32_f16 v[90:93], v[152:155], v[180:183], v[90:93]
	v_mfma_f32_16x16x32_f16 v[62:65], v[152:155], v[228:231], v[62:65]
	s_waitcnt vmcnt(17)
	v_mfma_f32_16x16x32_f16 v[38:41], v[224:227], v[46:49], v[38:41]
	v_mfma_f32_16x16x32_f16 v[42:45], v[224:227], v[176:179], v[42:45]
	v_mfma_f32_16x16x32_f16 v[46:49], v[224:227], v[180:183], v[50:53]
	s_nop 2
	buffer_load_dwordx4 v[50:53], v147, s[16:19], s8 offen
	buffer_load_dwordx4 v[140:143], v148, s[16:19], s8 offen
	buffer_load_dwordx4 v[152:155], v149, s[16:19], s8 offen
	buffer_load_dwordx4 v[176:179], v150, s[16:19], s8 offen
	v_mfma_f32_16x16x32_f16 v[94:97], v[220:223], v[180:183], v[94:97]
	v_mfma_f32_16x16x32_f16 v[70:73], v[220:223], v[228:231], v[70:73]
	v_mfma_f32_16x16x32_f16 v[34:37], v[224:227], v[228:231], v[34:37]
	ds_read_b128 v[180:183], v100 offset:256
	ds_read_b128 v[220:223], v100 offset:16640
	ds_read_b128 v[224:227], v100 offset:33024
	ds_read_b128 v[228:231], v100 offset:49408
	s_add_i32 s8, s22, 0xfffb8000
	s_waitcnt vmcnt(15) lgkmcnt(7)
	v_mfma_f32_16x16x32_f16 v[164:167], v[126:129], v[204:207], v[164:167]
	s_waitcnt lgkmcnt(6)
	v_mfma_f32_16x16x32_f16 v[168:171], v[126:129], v[208:211], v[168:171]
	s_waitcnt lgkmcnt(5)
	v_mfma_f32_16x16x32_f16 v[172:175], v[126:129], v[212:215], v[172:175]
	s_waitcnt lgkmcnt(4)
	v_mfma_f32_16x16x32_f16 v[82:85], v[126:129], v[216:219], v[82:85]
	s_waitcnt vmcnt(14)
	v_mfma_f32_16x16x32_f16 v[58:61], v[136:139], v[204:207], v[58:61]
	v_mfma_f32_16x16x32_f16 v[86:89], v[136:139], v[208:211], v[86:89]
	v_mfma_f32_16x16x32_f16 v[94:97], v[136:139], v[212:215], v[94:97]
	v_mfma_f32_16x16x32_f16 v[70:73], v[136:139], v[216:219], v[70:73]
	s_waitcnt vmcnt(13)
	v_mfma_f32_16x16x32_f16 v[54:57], v[184:187], v[204:207], v[54:57]
	v_mfma_f32_16x16x32_f16 v[74:77], v[184:187], v[208:211], v[74:77]
	v_mfma_f32_16x16x32_f16 v[90:93], v[184:187], v[212:215], v[90:93]
	v_mfma_f32_16x16x32_f16 v[62:65], v[184:187], v[216:219], v[62:65]
	s_waitcnt vmcnt(12)
	v_mfma_f32_16x16x32_f16 v[38:41], v[188:191], v[204:207], v[38:41]
	buffer_load_dwordx4 v[126:129], v147, s[16:19], s8 offen
	buffer_load_dwordx4 v[136:139], v148, s[16:19], s8 offen
	buffer_load_dwordx4 v[184:187], v149, s[16:19], s8 offen
	buffer_load_dwordx4 v[204:207], v150, s[16:19], s8 offen
	v_mfma_f32_16x16x32_f16 v[42:45], v[188:191], v[208:211], v[42:45]
	v_mfma_f32_16x16x32_f16 v[46:49], v[188:191], v[212:215], v[46:49]
	v_mfma_f32_16x16x32_f16 v[34:37], v[188:191], v[216:219], v[34:37]
	ds_read_b128 v[188:191], v111 offset:512
	ds_read_b128 v[208:211], v111 offset:16896
	ds_read_b128 v[212:215], v111 offset:33280
	ds_read_b128 v[216:219], v111 offset:49664
	s_add_i32 s8, s22, 0xfffc0000
	s_waitcnt vmcnt(15) lgkmcnt(7)
	v_mfma_f32_16x16x32_f16 v[164:167], v[78:81], v[180:183], v[164:167]
	s_waitcnt lgkmcnt(6)
	v_mfma_f32_16x16x32_f16 v[168:171], v[78:81], v[220:223], v[168:171]
	s_waitcnt lgkmcnt(5)
	v_mfma_f32_16x16x32_f16 v[172:175], v[78:81], v[224:227], v[172:175]
	s_waitcnt lgkmcnt(4)
	v_mfma_f32_16x16x32_f16 v[78:81], v[78:81], v[228:231], v[82:85]
	s_waitcnt vmcnt(14)
	v_mfma_f32_16x16x32_f16 v[58:61], v[122:125], v[180:183], v[58:61]
	v_mfma_f32_16x16x32_f16 v[82:85], v[122:125], v[220:223], v[86:89]
	v_mfma_f32_16x16x32_f16 v[86:89], v[122:125], v[224:227], v[94:97]
	v_mfma_f32_16x16x32_f16 v[70:73], v[122:125], v[228:231], v[70:73]
	s_waitcnt vmcnt(13)
	v_mfma_f32_16x16x32_f16 v[54:57], v[156:159], v[180:183], v[54:57]
	v_mfma_f32_16x16x32_f16 v[74:77], v[156:159], v[220:223], v[74:77]
	v_mfma_f32_16x16x32_f16 v[90:93], v[156:159], v[224:227], v[90:93]
	v_mfma_f32_16x16x32_f16 v[62:65], v[156:159], v[228:231], v[62:65]
	s_waitcnt vmcnt(12)
	v_mfma_f32_16x16x32_f16 v[38:41], v[160:163], v[180:183], v[38:41]
	buffer_load_dwordx4 v[94:97], v147, s[16:19], s8 offen
	buffer_load_dwordx4 v[122:125], v148, s[16:19], s8 offen
	buffer_load_dwordx4 v[156:159], v149, s[16:19], s8 offen
	buffer_load_dwordx4 v[180:183], v150, s[16:19], s8 offen
	v_mfma_f32_16x16x32_f16 v[42:45], v[160:163], v[220:223], v[42:45]
	v_mfma_f32_16x16x32_f16 v[46:49], v[160:163], v[224:227], v[46:49]
	v_mfma_f32_16x16x32_f16 v[34:37], v[160:163], v[228:231], v[34:37]
	ds_read_b128 v[160:163], v98 offset:512
	ds_read_b128 v[220:223], v98 offset:16896
	ds_read_b128 v[224:227], v98 offset:33280
	ds_read_b128 v[228:231], v98 offset:49664
	s_add_i32 s8, s22, 0xfffc8000
	s_waitcnt vmcnt(15) lgkmcnt(7)
	v_mfma_f32_16x16x32_f16 v[164:167], v[66:69], v[188:191], v[164:167]
	s_waitcnt lgkmcnt(6)
	v_mfma_f32_16x16x32_f16 v[168:171], v[66:69], v[208:211], v[168:171]
	s_waitcnt lgkmcnt(5)
	v_mfma_f32_16x16x32_f16 v[172:175], v[66:69], v[212:215], v[172:175]
	s_waitcnt lgkmcnt(4)
	v_mfma_f32_16x16x32_f16 v[66:69], v[66:69], v[216:219], v[78:81]
	s_waitcnt vmcnt(14)
	v_mfma_f32_16x16x32_f16 v[58:61], v[192:195], v[188:191], v[58:61]
	v_mfma_f32_16x16x32_f16 v[78:81], v[192:195], v[208:211], v[82:85]
	v_mfma_f32_16x16x32_f16 v[82:85], v[192:195], v[212:215], v[86:89]
	v_mfma_f32_16x16x32_f16 v[70:73], v[192:195], v[216:219], v[70:73]
	s_waitcnt vmcnt(13)
	v_mfma_f32_16x16x32_f16 v[54:57], v[196:199], v[188:191], v[54:57]
	v_mfma_f32_16x16x32_f16 v[74:77], v[196:199], v[208:211], v[74:77]
	v_mfma_f32_16x16x32_f16 v[86:89], v[196:199], v[212:215], v[90:93]
	v_mfma_f32_16x16x32_f16 v[62:65], v[196:199], v[216:219], v[62:65]
	s_waitcnt vmcnt(12)
	v_mfma_f32_16x16x32_f16 v[38:41], v[200:203], v[188:191], v[38:41]
	buffer_load_dwordx4 v[90:93], v147, s[16:19], s8 offen
	buffer_load_dwordx4 v[188:191], v148, s[16:19], s8 offen
	buffer_load_dwordx4 v[192:195], v149, s[16:19], s8 offen
	buffer_load_dwordx4 v[196:199], v150, s[16:19], s8 offen
	v_mfma_f32_16x16x32_f16 v[42:45], v[200:203], v[208:211], v[42:45]
	v_mfma_f32_16x16x32_f16 v[46:49], v[200:203], v[212:215], v[46:49]
	v_mfma_f32_16x16x32_f16 v[34:37], v[200:203], v[216:219], v[34:37]
	ds_read_b128 v[200:203], v99 offset:512
	ds_read_b128 v[208:211], v99 offset:16896
	ds_read_b128 v[212:215], v99 offset:33280
	ds_read_b128 v[216:219], v99 offset:49664
	s_add_i32 s8, s22, 0xfffd0000
	s_waitcnt vmcnt(15) lgkmcnt(7)
	v_mfma_f32_16x16x32_f16 v[164:167], v[50:53], v[160:163], v[164:167]
	s_waitcnt lgkmcnt(6)
	v_mfma_f32_16x16x32_f16 v[168:171], v[50:53], v[220:223], v[168:171]
	s_waitcnt lgkmcnt(5)
	v_mfma_f32_16x16x32_f16 v[172:175], v[50:53], v[224:227], v[172:175]
	s_waitcnt lgkmcnt(4)
	v_mfma_f32_16x16x32_f16 v[50:53], v[50:53], v[228:231], v[66:69]
	s_waitcnt vmcnt(14)
	v_mfma_f32_16x16x32_f16 v[58:61], v[140:143], v[160:163], v[58:61]
	v_mfma_f32_16x16x32_f16 v[66:69], v[140:143], v[220:223], v[78:81]
	v_mfma_f32_16x16x32_f16 v[78:81], v[140:143], v[224:227], v[82:85]
	v_mfma_f32_16x16x32_f16 v[70:73], v[140:143], v[228:231], v[70:73]
	s_waitcnt vmcnt(13)
	v_mfma_f32_16x16x32_f16 v[54:57], v[152:155], v[160:163], v[54:57]
	v_mfma_f32_16x16x32_f16 v[74:77], v[152:155], v[220:223], v[74:77]
	v_mfma_f32_16x16x32_f16 v[82:85], v[152:155], v[224:227], v[86:89]
	v_mfma_f32_16x16x32_f16 v[62:65], v[152:155], v[228:231], v[62:65]
	s_waitcnt vmcnt(12)
	v_mfma_f32_16x16x32_f16 v[38:41], v[176:179], v[160:163], v[38:41]
	buffer_load_dwordx4 v[86:89], v147, s[16:19], s8 offen
	buffer_load_dwordx4 v[140:143], v148, s[16:19], s8 offen
	buffer_load_dwordx4 v[152:155], v149, s[16:19], s8 offen
	buffer_load_dwordx4 v[160:163], v150, s[16:19], s8 offen
	v_mfma_f32_16x16x32_f16 v[42:45], v[176:179], v[220:223], v[42:45]
	v_mfma_f32_16x16x32_f16 v[46:49], v[176:179], v[224:227], v[46:49]
	v_mfma_f32_16x16x32_f16 v[34:37], v[176:179], v[228:231], v[34:37]
	ds_read_b128 v[176:179], v100 offset:512
	ds_read_b128 v[220:223], v100 offset:16896
	ds_read_b128 v[224:227], v100 offset:33280
	ds_read_b128 v[228:231], v100 offset:49664
	s_add_i32 s8, s22, 0xfffd8000
	s_waitcnt vmcnt(15) lgkmcnt(7)
	v_mfma_f32_16x16x32_f16 v[164:167], v[126:129], v[200:203], v[164:167]
	s_waitcnt lgkmcnt(6)
	v_mfma_f32_16x16x32_f16 v[168:171], v[126:129], v[208:211], v[168:171]
	s_waitcnt lgkmcnt(5)
	v_mfma_f32_16x16x32_f16 v[172:175], v[126:129], v[212:215], v[172:175]
	s_waitcnt lgkmcnt(4)
	v_mfma_f32_16x16x32_f16 v[50:53], v[126:129], v[216:219], v[50:53]
	s_waitcnt vmcnt(14)
	v_mfma_f32_16x16x32_f16 v[58:61], v[136:139], v[200:203], v[58:61]
	v_mfma_f32_16x16x32_f16 v[66:69], v[136:139], v[208:211], v[66:69]
	v_mfma_f32_16x16x32_f16 v[78:81], v[136:139], v[212:215], v[78:81]
	v_mfma_f32_16x16x32_f16 v[70:73], v[136:139], v[216:219], v[70:73]
	s_waitcnt vmcnt(13)
	v_mfma_f32_16x16x32_f16 v[54:57], v[184:187], v[200:203], v[54:57]
	v_mfma_f32_16x16x32_f16 v[74:77], v[184:187], v[208:211], v[74:77]
	v_mfma_f32_16x16x32_f16 v[82:85], v[184:187], v[212:215], v[82:85]
	v_mfma_f32_16x16x32_f16 v[62:65], v[184:187], v[216:219], v[62:65]
	s_waitcnt vmcnt(12)
	v_mfma_f32_16x16x32_f16 v[38:41], v[204:207], v[200:203], v[38:41]
	buffer_load_dwordx4 v[126:129], v147, s[16:19], s8 offen
	buffer_load_dwordx4 v[136:139], v148, s[16:19], s8 offen
	buffer_load_dwordx4 v[184:187], v149, s[16:19], s8 offen
	buffer_load_dwordx4 v[200:203], v150, s[16:19], s8 offen
	v_mfma_f32_16x16x32_f16 v[42:45], v[204:207], v[208:211], v[42:45]
	v_mfma_f32_16x16x32_f16 v[46:49], v[204:207], v[212:215], v[46:49]
	v_mfma_f32_16x16x32_f16 v[34:37], v[204:207], v[216:219], v[34:37]
	ds_read_b128 v[204:207], v111 offset:768
	ds_read_b128 v[208:211], v111 offset:17152
	ds_read_b128 v[212:215], v111 offset:33536
	ds_read_b128 v[216:219], v111 offset:49920
	s_add_i32 s8, s22, 0xfffe0000
	s_waitcnt vmcnt(15) lgkmcnt(7)
	v_mfma_f32_16x16x32_f16 v[164:167], v[94:97], v[176:179], v[164:167]
	s_waitcnt lgkmcnt(6)
	v_mfma_f32_16x16x32_f16 v[168:171], v[94:97], v[220:223], v[168:171]
	s_waitcnt vmcnt(14)
	v_mfma_f32_16x16x32_f16 v[58:61], v[122:125], v[176:179], v[58:61]
	v_mfma_f32_16x16x32_f16 v[66:69], v[122:125], v[220:223], v[66:69]
	s_waitcnt lgkmcnt(5)
	v_mfma_f32_16x16x32_f16 v[78:81], v[122:125], v[224:227], v[78:81]
	s_waitcnt lgkmcnt(4)
	v_mfma_f32_16x16x32_f16 v[70:73], v[122:125], v[228:231], v[70:73]
	s_waitcnt vmcnt(13)
	v_mfma_f32_16x16x32_f16 v[54:57], v[156:159], v[176:179], v[54:57]
	v_mfma_f32_16x16x32_f16 v[74:77], v[156:159], v[220:223], v[74:77]
	v_mfma_f32_16x16x32_f16 v[82:85], v[156:159], v[224:227], v[82:85]
	v_mfma_f32_16x16x32_f16 v[62:65], v[156:159], v[228:231], v[62:65]
	s_waitcnt vmcnt(12)
	v_mfma_f32_16x16x32_f16 v[38:41], v[180:183], v[176:179], v[38:41]
	v_mfma_f32_16x16x32_f16 v[42:45], v[180:183], v[220:223], v[42:45]
	buffer_load_dwordx4 v[122:125], v147, s[16:19], s8 offen
	buffer_load_dwordx4 v[156:159], v148, s[16:19], s8 offen
	buffer_load_dwordx4 v[176:179], v149, s[16:19], s8 offen
	buffer_load_dwordx4 v[220:223], v150, s[16:19], s8 offen
	v_mfma_f32_16x16x32_f16 v[50:53], v[94:97], v[228:231], v[50:53]
	v_mfma_f32_16x16x32_f16 v[46:49], v[180:183], v[224:227], v[46:49]
	v_mfma_f32_16x16x32_f16 v[34:37], v[180:183], v[228:231], v[34:37]
	v_mfma_f32_16x16x32_f16 v[172:175], v[94:97], v[224:227], v[172:175]
	ds_read_b128 v[94:97], v98 offset:768
	ds_read_b128 v[180:183], v98 offset:17152
	ds_read_b128 v[224:227], v98 offset:33536
	ds_read_b128 v[228:231], v98 offset:49920
	s_add_i32 s8, s22, 0xfffe8000
	s_waitcnt vmcnt(15) lgkmcnt(7)
	v_mfma_f32_16x16x32_f16 v[164:167], v[90:93], v[204:207], v[164:167]
	s_waitcnt lgkmcnt(6)
	v_mfma_f32_16x16x32_f16 v[168:171], v[90:93], v[208:211], v[168:171]
	s_waitcnt lgkmcnt(5)
	v_mfma_f32_16x16x32_f16 v[172:175], v[90:93], v[212:215], v[172:175]
	s_waitcnt lgkmcnt(4)
	v_mfma_f32_16x16x32_f16 v[90:93], v[90:93], v[216:219], v[50:53]
	s_waitcnt vmcnt(14)
	v_mfma_f32_16x16x32_f16 v[232:235], v[188:191], v[204:207], v[58:61]
	v_mfma_f32_16x16x32_f16 v[66:69], v[188:191], v[208:211], v[66:69]
	v_mfma_f32_16x16x32_f16 v[78:81], v[188:191], v[212:215], v[78:81]
	v_mfma_f32_16x16x32_f16 v[70:73], v[188:191], v[216:219], v[70:73]
	s_waitcnt vmcnt(13)
	v_mfma_f32_16x16x32_f16 v[188:191], v[192:195], v[204:207], v[54:57]
	v_mfma_f32_16x16x32_f16 v[74:77], v[192:195], v[208:211], v[74:77]
	v_mfma_f32_16x16x32_f16 v[82:85], v[192:195], v[212:215], v[82:85]
	v_mfma_f32_16x16x32_f16 v[62:65], v[192:195], v[216:219], v[62:65]
	s_waitcnt vmcnt(12)
	v_mfma_f32_16x16x32_f16 v[192:195], v[196:199], v[204:207], v[38:41]
	buffer_load_dwordx4 v[58:61], v147, s[16:19], s8 offen
	buffer_load_dwordx4 v[54:57], v148, s[16:19], s8 offen
	buffer_load_dwordx4 v[50:53], v149, s[16:19], s8 offen
	buffer_load_dwordx4 v[38:41], v150, s[16:19], s8 offen
	v_mfma_f32_16x16x32_f16 v[42:45], v[196:199], v[208:211], v[42:45]
	v_mfma_f32_16x16x32_f16 v[46:49], v[196:199], v[212:215], v[46:49]
	v_mfma_f32_16x16x32_f16 v[196:199], v[196:199], v[216:219], v[34:37]
	ds_read_b128 v[204:207], v99 offset:768
	ds_read_b128 v[208:211], v99 offset:17152
	ds_read_b128 v[212:215], v99 offset:33536
	ds_read_b128 v[216:219], v99 offset:49920
	s_add_i32 s8, s22, 0xffff0000
	s_waitcnt vmcnt(15) lgkmcnt(7)
	v_mfma_f32_16x16x32_f16 v[164:167], v[86:89], v[94:97], v[164:167]
	s_waitcnt lgkmcnt(6)
	v_mfma_f32_16x16x32_f16 v[168:171], v[86:89], v[180:183], v[168:171]
	s_waitcnt lgkmcnt(5)
	v_mfma_f32_16x16x32_f16 v[172:175], v[86:89], v[224:227], v[172:175]
	s_waitcnt lgkmcnt(4)
	v_mfma_f32_16x16x32_f16 v[86:89], v[86:89], v[228:231], v[90:93]
	s_waitcnt vmcnt(14)
	v_mfma_f32_16x16x32_f16 v[232:235], v[140:143], v[94:97], v[232:235]
	v_mfma_f32_16x16x32_f16 v[66:69], v[140:143], v[180:183], v[66:69]
	v_mfma_f32_16x16x32_f16 v[236:239], v[140:143], v[224:227], v[78:81]
	v_mfma_f32_16x16x32_f16 v[70:73], v[140:143], v[228:231], v[70:73]
	s_waitcnt vmcnt(13)
	v_mfma_f32_16x16x32_f16 v[140:143], v[152:155], v[94:97], v[188:191]
	v_mfma_f32_16x16x32_f16 v[74:77], v[152:155], v[180:183], v[74:77]
	v_mfma_f32_16x16x32_f16 v[82:85], v[152:155], v[224:227], v[82:85]
	v_mfma_f32_16x16x32_f16 v[62:65], v[152:155], v[228:231], v[62:65]
	s_waitcnt vmcnt(12)
	v_mfma_f32_16x16x32_f16 v[152:155], v[160:163], v[94:97], v[192:195]
	buffer_load_dwordx4 v[94:97], v147, s[16:19], s8 offen
	buffer_load_dwordx4 v[90:93], v148, s[16:19], s8 offen
	buffer_load_dwordx4 v[78:81], v149, s[16:19], s8 offen
	buffer_load_dwordx4 v[34:37], v150, s[16:19], s8 offen
	v_mfma_f32_16x16x32_f16 v[42:45], v[160:163], v[180:183], v[42:45]
	v_mfma_f32_16x16x32_f16 v[46:49], v[160:163], v[224:227], v[46:49]
	v_mfma_f32_16x16x32_f16 v[160:163], v[160:163], v[228:231], v[196:199]
	ds_read_b128 v[180:183], v100 offset:768
	ds_read_b128 v[188:191], v100 offset:17152
	ds_read_b128 v[192:195], v100 offset:33536
	ds_read_b128 v[196:199], v100 offset:49920
	s_add_i32 s8, s22, 0xffff8000
	s_waitcnt vmcnt(15) lgkmcnt(7)
	v_mfma_f32_16x16x32_f16 v[164:167], v[126:129], v[204:207], v[164:167]
	s_waitcnt lgkmcnt(6)
	v_mfma_f32_16x16x32_f16 v[168:171], v[126:129], v[208:211], v[168:171]
	s_waitcnt lgkmcnt(5)
	v_mfma_f32_16x16x32_f16 v[172:175], v[126:129], v[212:215], v[172:175]
	s_waitcnt lgkmcnt(4)
	v_mfma_f32_16x16x32_f16 v[86:89], v[126:129], v[216:219], v[86:89]
	s_waitcnt vmcnt(14)
	v_mfma_f32_16x16x32_f16 v[126:129], v[136:139], v[204:207], v[232:235]
	v_mfma_f32_16x16x32_f16 v[66:69], v[136:139], v[208:211], v[66:69]
	v_mfma_f32_16x16x32_f16 v[224:227], v[136:139], v[212:215], v[236:239]
	v_mfma_f32_16x16x32_f16 v[136:139], v[136:139], v[216:219], v[70:73]
	s_waitcnt vmcnt(13)
	v_mfma_f32_16x16x32_f16 v[140:143], v[184:187], v[204:207], v[140:143]
	v_mfma_f32_16x16x32_f16 v[74:77], v[184:187], v[208:211], v[74:77]
	v_mfma_f32_16x16x32_f16 v[228:231], v[184:187], v[212:215], v[82:85]
	v_mfma_f32_16x16x32_f16 v[184:187], v[184:187], v[216:219], v[62:65]
	s_waitcnt vmcnt(12)
	v_mfma_f32_16x16x32_f16 v[152:155], v[200:203], v[204:207], v[152:155]
	v_mfma_f32_16x16x32_f16 v[204:207], v[200:203], v[208:211], v[42:45]
	buffer_load_dwordx4 v[82:85], v147, s[16:19], s8 offen
	buffer_load_dwordx4 v[70:73], v148, s[16:19], s8 offen
	buffer_load_dwordx4 v[62:65], v149, s[16:19], s8 offen
	buffer_load_dwordx4 v[42:45], v150, s[16:19], s8 offen
	v_mfma_f32_16x16x32_f16 v[46:49], v[200:203], v[212:215], v[46:49]
	v_mfma_f32_16x16x32_f16 v[160:163], v[200:203], v[216:219], v[160:163]
	v_add_u32_e32 v0, 0x1ac00, v104
	ds_read_b128 v[240:243], v0
	ds_read_b128 v[244:247], v0 offset:16
	s_waitcnt vmcnt(12) lgkmcnt(5)
	v_mfma_f32_16x16x32_f16 v[164:167], v[122:125], v[180:183], v[164:167]
	v_mfma_f32_16x16x32_f16 v[126:129], v[156:159], v[180:183], v[126:129]
	v_mfma_f32_16x16x32_f16 v[140:143], v[176:179], v[180:183], v[140:143]
	v_mfma_f32_16x16x32_f16 v[152:155], v[220:223], v[180:183], v[152:155]
	s_waitcnt lgkmcnt(4)
	v_mfma_f32_16x16x32_f16 v[168:171], v[122:125], v[188:191], v[168:171]
	v_mfma_f32_16x16x32_f16 v[208:211], v[156:159], v[188:191], v[66:69]
	v_mfma_f32_16x16x32_f16 v[212:215], v[176:179], v[188:191], v[74:77]
	v_mfma_f32_16x16x32_f16 v[204:207], v[220:223], v[188:191], v[204:207]
	s_waitcnt lgkmcnt(3)
	v_mfma_f32_16x16x32_f16 v[172:175], v[122:125], v[192:195], v[172:175]
	v_cvt_pk_f16_f32 v232, v164, v165
	v_cvt_pk_f16_f32 v233, v166, v167
	v_pk_max_f16 v232, v232, 0
	v_pk_max_f16 v233, v233, 0
	v_mfma_f32_16x16x32_f16 v[224:227], v[156:159], v[192:195], v[224:227]
	v_cvt_pk_f16_f32 v234, v126, v127
	v_cvt_pk_f16_f32 v235, v128, v129
	v_pk_max_f16 v234, v234, 0
	v_pk_max_f16 v235, v235, 0
	v_mfma_f32_16x16x32_f16 v[228:231], v[176:179], v[192:195], v[228:231]
	v_cvt_pk_f16_f32 v236, v140, v141
	v_cvt_pk_f16_f32 v237, v142, v143
	v_pk_max_f16 v236, v236, 0
	v_pk_max_f16 v237, v237, 0
	v_mfma_f32_16x16x32_f16 v[216:219], v[220:223], v[192:195], v[46:49]
	v_cvt_pk_f16_f32 v238, v152, v153
	v_cvt_pk_f16_f32 v239, v154, v155
	v_pk_max_f16 v238, v238, 0
	v_pk_max_f16 v239, v239, 0
	s_waitcnt lgkmcnt(2)
	v_mfma_f32_16x16x32_f16 v[200:203], v[122:125], v[196:199], v[86:89]
	v_cvt_pk_f16_f32 v180, v168, v169
	v_cvt_pk_f16_f32 v181, v170, v171
	v_pk_max_f16 v180, v180, 0
	v_pk_max_f16 v181, v181, 0
	buffer_load_dwordx4 v[86:89], v147, s[16:19], s22 offen
	buffer_load_dwordx4 v[74:77], v148, s[16:19], s22 offen
	buffer_load_dwordx4 v[66:69], v149, s[16:19], s22 offen
	buffer_load_dwordx4 v[46:49], v150, s[16:19], s22 offen
	v_mfma_f32_16x16x32_f16 v[136:139], v[156:159], v[196:199], v[136:139]
	v_cvt_pk_f16_f32 v182, v208, v209
	v_cvt_pk_f16_f32 v183, v210, v211
	v_pk_max_f16 v182, v182, 0
	v_pk_max_f16 v183, v183, 0
	s_waitcnt lgkmcnt(1)
	v_mfma_f32_16x16x32_f16 v[252:255], v[240:243], v[232:235], 0
	v_cvt_pk_f16_f32 v232, v172, v173
	v_cvt_pk_f16_f32 v233, v174, v175
	v_pk_max_f16 v232, v232, 0
	v_pk_max_f16 v233, v233, 0
	v_mfma_f32_16x16x32_f16 v[184:187], v[176:179], v[196:199], v[184:187]
	v_cvt_pk_f16_f32 v188, v212, v213
	v_cvt_pk_f16_f32 v189, v214, v215
	v_pk_max_f16 v188, v188, 0
	v_pk_max_f16 v189, v189, 0
	s_waitcnt lgkmcnt(0)
	v_mfma_f32_16x16x32_f16 v[252:255], v[244:247], v[236:239], v[252:255]
	v_cvt_pk_f16_f32 v234, v224, v225
	v_cvt_pk_f16_f32 v235, v226, v227
	v_pk_max_f16 v234, v234, 0
	v_pk_max_f16 v235, v235, 0
	v_mfma_f32_16x16x32_f16 v[160:163], v[220:223], v[196:199], v[160:163]
	v_cvt_pk_f16_f32 v190, v204, v205
	v_cvt_pk_f16_f32 v191, v206, v207
	v_pk_max_f16 v190, v190, 0
	v_pk_max_f16 v191, v191, 0
	v_mfma_f32_16x16x32_f16 v[192:195], v[240:243], v[180:183], 0
	v_cvt_pk_f16_f32 v236, v228, v229
	v_cvt_pk_f16_f32 v237, v230, v231
	v_pk_max_f16 v236, v236, 0
	v_pk_max_f16 v237, v237, 0
	v_mfma_f32_16x16x32_f16 v[192:195], v[244:247], v[188:191], v[192:195]
	v_cvt_pk_f16_f32 v238, v216, v217
	v_cvt_pk_f16_f32 v239, v218, v219
	v_pk_max_f16 v238, v238, 0
	v_pk_max_f16 v239, v239, 0
	v_cvt_pk_f16_f32 v180, v200, v201
	v_cvt_pk_f16_f32 v181, v202, v203
	v_pk_max_f16 v180, v180, 0
	v_pk_max_f16 v181, v181, 0
	v_mfma_f32_16x16x32_f16 v[196:199], v[240:243], v[232:235], 0
	v_cvt_pk_f16_f32 v182, v136, v137
	v_cvt_pk_f16_f32 v183, v138, v139
	v_pk_max_f16 v182, v182, 0
	v_pk_max_f16 v183, v183, 0
	v_mfma_f32_16x16x32_f16 v[196:199], v[244:247], v[236:239], v[196:199]
	v_cvt_pk_f16_f32 v188, v184, v185
	v_cvt_pk_f16_f32 v189, v186, v187
	v_pk_max_f16 v188, v188, 0
	v_pk_max_f16 v189, v189, 0
	v_cvt_pk_f16_f32 v190, v160, v161
	v_cvt_pk_f16_f32 v191, v162, v163
	v_pk_max_f16 v190, v190, 0
	v_pk_max_f16 v191, v191, 0
	v_mfma_f32_16x16x32_f16 v[122:125], v[240:243], v[180:183], 0
	s_nop 0
	v_mfma_f32_16x16x32_f16 v[122:125], v[244:247], v[188:191], v[122:125]
	v_add_u32_e32 v145, 0x12c00, v105
	ds_read_b128 v[240:243], v145 offset:2048
	ds_read_b128 v[244:247], v145 offset:2064
	ds_read_b128 v[248:251], v145 offset:2080
	s_load_dword s30, s[12:13], 0x0
	v_cndmask_b32_e64 v0, v252, v192, s[2:3]
	ds_read_b128 v[252:255], v145 offset:2096
	ds_read_u16 v102, v114
	ds_read_u16 v103, v114 offset:512
	ds_read_u16 v115, v114 offset:1024
	ds_read_u16 v116, v114 offset:1536
	v_cndmask_b32_e64 v0, v0, v196, s[0:1]
	s_waitcnt vmcnt(16)
	v_cndmask_b32_e64 v1, v30, v134, s[0:1]
	v_bfi_b32 v30, s10, v1, v30
	v_perm_b32 v1, v22, v134, s24
	v_cndmask_b32_e64 v22, v22, v1, s[0:1]
	v_bfi_b32 v1, s10, v135, v18
	v_perm_b32 v121, v10, v135, s24
	v_cndmask_b32_e64 v18, v18, v1, s[0:1]
	v_cndmask_b32_e64 v10, v10, v121, s[0:1]
	v_cndmask_b32_e64 v0, v0, v122, s[26:27]
	ds_write_b32 v112, v0
	s_add_i32 s22, s22, 0x80000
	s_add_i32 s11, s11, 1
	s_add_u32 s12, s12, 4
	s_addc_u32 s13, s13, 0
	v_add_u32_e32 v104, 0x400, v104
	v_add_u32_e32 v105, 0x800, v105
	v_add_u32_e32 v114, 2, v114
	s_cmp_eq_u32 s22, 0x898000
	s_waitcnt lgkmcnt(0)
	s_barrier
	ds_read_b128 v[232:235], v113
	ds_read_b128 v[236:239], v113 offset:1024
	s_waitcnt lgkmcnt(0)
	v_add_f32_e32 v0, v232, v233
	v_add_f32_e32 v1, v234, v235
	v_add_f32_e32 v121, v236, v237
	v_add_f32_e32 v144, v238, v239
	v_add_f32_e32 v0, v0, v1
	v_add_f32_e32 v121, v121, v144
	v_add_f32_e32 v0, v0, v121
	v_add_f32_e32 v0, s30, v0
	ds_write_b32 v106, v0
	v_cvt_f16_f32_e32 v1, v0
	v_cvt_f16_f32_e32 v121, v0
	s_nop 1
	v_permlane16_swap_b32_e32 v1, v121
	v_mov_b32_e32 v144, v1
	v_mov_b32_e32 v145, v121
	s_nop 1
	v_permlane32_swap_b32_e32 v1, v144
	v_permlane32_swap_b32_e32 v121, v145
	v_add_u32_e32 v106, 4, v106
	s_cbranch_scc0 .LBB1_4
